# static s_setprio 1 for waves 0-3 (older half) instead, per-segment flips deleted
# speedup vs baseline: 1.0064x; 1.0064x over previous
; #define LAS __attribute__((address_space(3)))
; __global__ void __launch_bounds__(NWAVES * 64, 2) fwd(P p) {
;     ...
;     const int tid = threadIdx.x, lane = tid & 63, wave = __builtin_amdgcn_readfirstlane(tid >> 6);
;     const int G = gridDim.x, bx = blockIdx.x; const int vcu = (G % 8 == 0) ? (bx % 8) * (G / 8) + bx / 8 : bx;
;     const int gw = vcu * NWAVES + wave, NGW = G * NWAVES;
;     for (int u = tid; u < (LDS_BYTES - LDSCTL_OFF) / 4; u += NWAVES * 64) ((LAS unsigned*)(lds + LDSCTL_OFF))[u] = 0u;
;     __syncthreads();
.LBB5_2:
	s_cmp_lt_u32 s16, 0x100
	s_cbranch_scc0 .Lprio_done
	s_setprio 1
